# v039 + MLA V LDS-DMA in saddr form: scalar tile pointer, no 64-bit vector adds left in the MLA softmax segment
# speedup vs baseline: 1.0063x; 1.0063x over previous
; __device__ __forceinline__ int kg(int row) { return (row >> 1) & 7; }
; __device__ __forceinline__ int v_rd_base(int lane) { return ((lane & 3) << 3) | (((lane >> 2) & 3) << 6) | (((lane >> 4) & 1) << 5) | (((lane >> 5) & 1) << 8); }
; #define BAR_ALL() asm volatile("s_waitcnt lgkmcnt(0)\n\ts_barrier" ::: "memory")
; #define DMA_K(tile, b) DMA_KP(Kh, tile, b)
; #define DMA_V(tile, b) DMA_VP(Vh, tile, b)
;     ...
;     float mhat = 0.f, l_reg = 0; bf16x8 qr[NQ];
; #pragma unroll
;     for (int d = 0; d < 4; ++d) o[d] = f32x16{};
;     const bf16_t* Qw = Qb + (long)((wid * QBLK + r32) * LDQ + hi * 8);
; #pragma unroll
;     for (int d0 = 0; d0 < NQ; ++d0) qr[d0] = *reinterpret_cast<const bf16x8*>(Qw + d0 * 16);
;     const int vb0 = (int)(uintptr_t)V_lds + v_rd_base(lane);
;     int ka[4];
; #pragma unroll
;     for (int b = 0; b < 4; ++b) ka[b] = (int)(uintptr_t)lds + r32 * RB + ((b * 32 + hi * 16) ^ (kg(r32) << 4));
;     f32x16 p0, p1; bf16x8 pa0, pa1, pa2, pa3;
;     asm volatile("s_waitcnt vmcnt(0)" ::: "memory"); BAR_ALL();
;     if (ATT_SKEW && g == 1) BAR_ALL();
;     ...
;     int ci = 0;
;     if (DMA_M) { DMA_K(2, 2); DMA_V(1, 1); }
;     SEG_M(true, false, 0, 0); BAR_ALL();
.LBB0_602:
	v_lshlrev_b32_e32 v26, 3, v200
	v_and_b32_e32 v23, 0xc0, v23
	s_cmp_lg_u32 0, -1
	v_and_or_b32 v23, v26, 24, v23
	v_and_b32_e32 v24, 32, v24
	v_and_b32_e32 v27, 0x100, v26
	s_cselect_b32 s10, 0, 0
	v_or3_b32 v23, v23, v24, v27
	v_mov_b32_e32 v24, s10
	s_movk_i32 s11, 0x180
	v_lshlrev_b32_e32 v177, 4, v25
	v_mad_u32_u24 v24, v22, s11, v24
	v_and_b32_e32 v25, 0x70, v26
	v_add_u32_e32 v26, 32, v177
	v_xad_u32 v187, v26, v25, v24
	v_add_u32_e32 v26, 64, v177
	v_xad_u32 v205, v26, v25, v24
	v_add_u32_e32 v26, 0x60, v177
	v_xad_u32 v185, v177, v25, v24
	v_xad_u32 v206, v26, v25, v24
	ds_read_b128 v[24:27], v185 offset:0
	ds_read_b128 v[28:31], v185 offset:0x3000
	ds_read_b128 v[32:35], v187 offset:0
	ds_read_b128 v[36:39], v187 offset:0x3000
	s_add_i32 s10, s10, 0x12000
	s_mov_b32 s26, 0
	v_add_u32_e32 v202, s10, v23
	v_mov_b64_e32 v[94:95], v[14:15]
	v_mov_b64_e32 v[92:93], v[12:13]
	v_mov_b64_e32 v[90:91], v[10:11]
	v_mov_b64_e32 v[88:89], v[8:9]
	v_mov_b64_e32 v[86:87], v[6:7]
	v_mov_b64_e32 v[84:85], v[4:5]
	v_mov_b64_e32 v[82:83], v[2:3]
	v_mov_b64_e32 v[80:81], v[0:1]
	s_waitcnt lgkmcnt(3)
	s_waitcnt vmcnt(0)
	s_nop 0
	v_mfma_f32_32x32x16_bf16 v[96:111], v[24:27], v[112:115], v[80:95]
	ds_read_b128 v[24:27], v205 offset:0
	s_waitcnt lgkmcnt(3)
	s_nop 0
	v_mfma_f32_32x32x16_bf16 v[80:95], v[28:31], v[112:115], v[80:95]
	ds_read_b128 v[28:31], v205 offset:0x3000
	s_waitcnt lgkmcnt(3)
	s_nop 0
	v_mfma_f32_32x32x16_bf16 v[96:111], v[32:35], v[116:119], v[96:111]
	ds_read_b128 v[32:35], v206 offset:0
	s_waitcnt lgkmcnt(3)
	s_nop 0
	v_mfma_f32_32x32x16_bf16 v[80:95], v[36:39], v[116:119], v[80:95]
	ds_read_b128 v[36:39], v206 offset:0x3000
	s_waitcnt lgkmcnt(3)
	s_nop 0
	v_mfma_f32_32x32x16_bf16 v[96:111], v[24:27], v[120:123], v[96:111]
	ds_read_b128 v[24:27], v185 offset:0x80
	s_waitcnt lgkmcnt(3)
	s_nop 0
	v_mfma_f32_32x32x16_bf16 v[80:95], v[28:31], v[120:123], v[80:95]
	ds_read_b128 v[28:31], v185 offset:0x3080
	s_waitcnt lgkmcnt(3)
	s_nop 0
	v_mfma_f32_32x32x16_bf16 v[96:111], v[32:35], v[124:127], v[96:111]
	ds_read_b128 v[32:35], v187 offset:0x80
	s_waitcnt lgkmcnt(3)
	s_nop 0
	v_mfma_f32_32x32x16_bf16 v[80:95], v[36:39], v[124:127], v[80:95]
	ds_read_b128 v[36:39], v187 offset:0x3080
	s_waitcnt lgkmcnt(3)
	s_nop 0
	v_mfma_f32_32x32x16_bf16 v[96:111], v[24:27], v[128:131], v[96:111]
	ds_read_b128 v[24:27], v205 offset:0x80
	s_waitcnt lgkmcnt(3)
	s_nop 0
	v_mfma_f32_32x32x16_bf16 v[80:95], v[28:31], v[128:131], v[80:95]
	ds_read_b128 v[28:31], v205 offset:0x3080
	s_waitcnt lgkmcnt(3)
	s_nop 0
	v_mfma_f32_32x32x16_bf16 v[96:111], v[32:35], v[132:135], v[96:111]
	ds_read_b128 v[32:35], v206 offset:0x80
	s_waitcnt lgkmcnt(3)
	s_nop 0
	v_mfma_f32_32x32x16_bf16 v[80:95], v[36:39], v[132:135], v[80:95]
	ds_read_b128 v[36:39], v206 offset:0x3080
	s_waitcnt lgkmcnt(3)
	s_nop 0
	v_mfma_f32_32x32x16_bf16 v[96:111], v[24:27], v[136:139], v[96:111]
	ds_read_b128 v[24:27], v185 offset:0x100
	s_waitcnt lgkmcnt(3)
	s_nop 0
	v_mfma_f32_32x32x16_bf16 v[80:95], v[28:31], v[136:139], v[80:95]
	ds_read_b128 v[28:31], v185 offset:0x3100
	s_waitcnt lgkmcnt(3)
	s_nop 0
	v_mfma_f32_32x32x16_bf16 v[96:111], v[32:35], v[140:143], v[96:111]
	ds_read_b128 v[32:35], v187 offset:0x100
	s_waitcnt lgkmcnt(3)
	s_nop 0
	v_mfma_f32_32x32x16_bf16 v[80:95], v[36:39], v[140:143], v[80:95]
	ds_read_b128 v[36:39], v187 offset:0x3100
	s_waitcnt lgkmcnt(3)
	s_nop 0
	v_mfma_f32_32x32x16_bf16 v[96:111], v[24:27], v[144:147], v[96:111]
	ds_read_b128 v[24:27], v205 offset:0x100
	s_waitcnt lgkmcnt(3)
	s_nop 0
	v_mfma_f32_32x32x16_bf16 v[80:95], v[28:31], v[144:147], v[80:95]
	ds_read_b128 v[28:31], v205 offset:0x3100
	s_waitcnt lgkmcnt(3)
	s_nop 0
	v_mfma_f32_32x32x16_bf16 v[96:111], v[32:35], v[148:151], v[96:111]
	ds_read_b128 v[32:35], v206 offset:0x100
	s_waitcnt lgkmcnt(3)
	s_nop 0
	v_mfma_f32_32x32x16_bf16 v[80:95], v[36:39], v[148:151], v[80:95]
	ds_read_b128 v[36:39], v206 offset:0x3100
	s_waitcnt lgkmcnt(3)
	s_nop 0
	v_mfma_f32_32x32x16_bf16 v[96:111], v[24:27], v[152:155], v[96:111]
	s_waitcnt lgkmcnt(2)
	s_nop 0
	v_mfma_f32_32x32x16_bf16 v[80:95], v[28:31], v[152:155], v[80:95]
	s_waitcnt lgkmcnt(1)
	s_nop 0
	v_mfma_f32_32x32x16_bf16 v[96:111], v[32:35], v[156:159], v[96:111]
	s_waitcnt lgkmcnt(0)
	s_nop 0
	v_mfma_f32_32x32x16_bf16 v[80:95], v[36:39], v[156:159], v[80:95]
	s_mul_i32 s53, s46, 0x180
	s_add_u32 s52, s52, s53
	s_addc_u32 s47, s47, 0
	s_add_u32 s52, s79, s52
	s_addc_u32 s53, s80, s47
	s_lshl_b32 s46, s46, 8
	s_add_u32 s44, s44, s46
	v_lshlrev_b32_e32 v20, 2, v20
	v_lshlrev_b32_e32 v17, 2, v17
	s_addc_u32 s45, s45, 0
	v_and_b32_e32 v20, 0xffffe000, v20
	v_lshlrev_b32_e32 v18, 10, v18
	v_and_b32_e32 v17, 0xffffe000, v17
	v_or3_b32 v20, v20, v18, v21
	s_add_u32 s44, s81, s44
	v_or3_b32 v17, v17, v18, v19
	s_waitcnt lgkmcnt(0)
	s_barrier
	v_add_u32_e32 v20, v20, v16
	v_mov_b32_e32 v21, v179
	s_addc_u32 s45, s82, s45
	v_add_u32_e32 v16, v17, v16
	v_mov_b32_e32 v17, v179
	v_mov_b32_e32 v64, v179
	v_mov_b32_e32 v65, v179
	v_lshl_add_u32 v201, v22, 2, s67
	v_mov_b32_e32 v181, v179
	v_mov_b32_e32 v183, v179
	v_mov_b32_e32 v228, v20
	v_mov_b32_e32 v229, v16
	s_mov_b64 s[100:101], s[44:45]
	v_mov_b32_e32 v66, v179
	v_mov_b32_e32 v67, v179
	v_mov_b32_e32 v68, v179
	v_mov_b32_e32 v69, v179
	v_mov_b32_e32 v70, v179
	v_mov_b32_e32 v71, v179
	v_mov_b32_e32 v72, v179
	v_mov_b32_e32 v73, v179
	v_mov_b32_e32 v74, v179
	v_mov_b32_e32 v75, v179
	v_mov_b32_e32 v76, v179
	v_mov_b32_e32 v77, v179
	v_mov_b32_e32 v78, v179
	v_mov_b32_e32 v79, v179
	v_mov_b64_e32 v[48:49], v[64:65]
	v_mov_b64_e32 v[32:33], v[64:65]
	v_mov_b64_e32 v[16:17], v[64:65]
	v_cmp_gt_u32_e64 s[10:11], 32, v200
	v_lshl_add_u64 v[188:189], s[52:53], 0, v[178:179]
	v_lshl_add_u64 v[190:191], s[52:53], 0, v[180:181]
	v_lshl_add_u64 v[192:193], s[52:53], 0, v[182:183]
	v_mov_b32_e32 v204, 0
	s_mov_b64 s[44:45], 0
	v_mov_b64_e32 v[50:51], v[66:67]
	v_mov_b64_e32 v[52:53], v[68:69]
	v_mov_b64_e32 v[54:55], v[70:71]
	v_mov_b64_e32 v[56:57], v[72:73]
	v_mov_b64_e32 v[58:59], v[74:75]
	v_mov_b64_e32 v[60:61], v[76:77]
	v_mov_b64_e32 v[62:63], v[78:79]
	v_mov_b64_e32 v[34:35], v[66:67]
	v_mov_b64_e32 v[36:37], v[68:69]
	v_mov_b64_e32 v[38:39], v[70:71]
	v_mov_b64_e32 v[40:41], v[72:73]
	v_mov_b64_e32 v[42:43], v[74:75]
	v_mov_b64_e32 v[44:45], v[76:77]
	v_mov_b64_e32 v[46:47], v[78:79]
	v_mov_b64_e32 v[18:19], v[66:67]
	v_mov_b64_e32 v[20:21], v[68:69]
	v_mov_b64_e32 v[22:23], v[70:71]
	v_mov_b64_e32 v[24:25], v[72:73]
	v_mov_b64_e32 v[26:27], v[74:75]
	v_mov_b64_e32 v[28:29], v[76:77]
	v_mov_b64_e32 v[30:31], v[78:79]
	v_mov_b32_e32 v203, 0
	s_branch .LBB0_606

; #define PK4(P, BASE, OUT) do { u32x4 w = {cvtpk(P[BASE + 0], P[BASE + 1]), cvtpk(P[BASE + 2], P[BASE + 3]), cvtpk(P[BASE + 4], P[BASE + 5]), cvtpk(P[BASE + 6], P[BASE + 7])}; \
;     OUT = *reinterpret_cast<bf16x8*>(&w); } while (0)
; __device__ __forceinline__ void smax_tile(f32x16& p0, f32x16& p1, float& mhat, float& l_reg, f32x16 (&o)[4], float* al_l, const bool first, int r32, int hi,
;                                           bf16x8& pa0, bf16x8& pa1, bf16x8& pa2, bf16x8& pa3) {
;     ...
; #pragma unroll
;     for (int r = 0; r < 16; ++r) p0[r] = __builtin_amdgcn_exp2f(p0[r]);
; #pragma unroll
;     for (int r = 0; r < 16; ++r) p1[r] = __builtin_amdgcn_exp2f(p1[r]);
;     float ps = p0[0];
; #pragma unroll
;     for (int r = 1; r < 16; ++r) ps += p0[r];
; #pragma unroll
;     for (int r = 0; r < 16; ++r) ps += p1[r];
;     { auto rr = __builtin_amdgcn_permlane32_swap(__float_as_uint(ps), __float_as_uint(ps), false, false); ps = __uint_as_float(rr[0]) + __uint_as_float(rr[1]); }
;     l_reg += ps;
;     ...
;     PK4(p0, 0, pa0); PK4(p0, 8, pa1); PK4(p1, 0, pa2); PK4(p1, 8, pa3);
.LBB0_605:
	v_exp_f32_e32 v96, v96
	v_exp_f32_e32 v97, v97
	v_exp_f32_e32 v98, v98
	v_exp_f32_e32 v99, v99
	v_exp_f32_e32 v100, v100
	v_exp_f32_e32 v101, v101
	v_add_f32_e32 v160, v96, v97
	v_exp_f32_e32 v102, v102
	v_add_f32_e32 v160, v98, v160
	v_exp_f32_e32 v103, v103
	v_add_f32_e32 v160, v99, v160
	v_exp_f32_e32 v104, v104
	v_add_f32_e32 v160, v100, v160
	v_exp_f32_e32 v105, v105
	v_add_f32_e32 v160, v101, v160
	v_exp_f32_e32 v106, v106
	v_add_f32_e32 v160, v102, v160
	v_exp_f32_e32 v107, v107
	v_add_f32_e32 v160, v103, v160
	v_exp_f32_e32 v108, v108
	v_add_f32_e32 v160, v104, v160
	v_exp_f32_e32 v109, v109
	v_add_f32_e32 v160, v105, v160
	v_exp_f32_e32 v110, v110
	v_add_f32_e32 v160, v106, v160
	v_exp_f32_e32 v111, v111
	v_add_f32_e32 v160, v107, v160
	v_exp_f32_e32 v80, v80
	v_add_f32_e32 v160, v108, v160
	v_exp_f32_e32 v81, v81
	v_add_f32_e32 v160, v109, v160
	v_exp_f32_e32 v82, v82
	v_add_f32_e32 v160, v110, v160
	v_exp_f32_e32 v83, v83
	v_add_f32_e32 v160, v111, v160
	v_exp_f32_e32 v84, v84
	v_add_f32_e32 v160, v80, v160
	v_exp_f32_e32 v85, v85
	v_add_f32_e32 v160, v81, v160
	v_exp_f32_e32 v86, v86
	v_add_f32_e32 v160, v82, v160
	v_exp_f32_e32 v87, v87
	v_add_f32_e32 v160, v83, v160
	v_exp_f32_e32 v88, v88
	v_add_f32_e32 v160, v84, v160
	v_exp_f32_e32 v89, v89
	v_add_f32_e32 v160, v85, v160
	v_exp_f32_e32 v90, v90
	v_add_f32_e32 v160, v86, v160
	v_exp_f32_e32 v91, v91
	v_add_f32_e32 v160, v87, v160
	v_exp_f32_e32 v92, v92
	v_add_f32_e32 v160, v88, v160
	v_exp_f32_e32 v93, v93
	v_add_f32_e32 v160, v89, v160
	v_exp_f32_e32 v94, v94
	v_add_f32_e32 v160, v90, v160
	v_exp_f32_e32 v95, v95
	v_add_f32_e32 v160, v91, v160
	v_add_f32_e32 v160, v92, v160
	v_add_f32_e32 v160, v93, v160
	v_add_f32_e32 v160, v94, v160
	v_add_f32_e32 v160, v95, v160
	v_mov_b32_e32 v161, v160
	v_cvt_pk_bf16_f32 v172, v96, v97
	v_cvt_pk_bf16_f32 v173, v98, v99
	v_permlane32_swap_b32_e32 v160, v161
	v_add_f32_e32 v160, v160, v161
	v_add_f32_e32 v204, v204, v160
	v_cvt_pk_bf16_f32 v174, v100, v101
	v_cvt_pk_bf16_f32 v175, v102, v103
	v_cvt_pk_bf16_f32 v168, v104, v105
	v_cvt_pk_bf16_f32 v169, v106, v107
	v_cvt_pk_bf16_f32 v170, v108, v109
	v_cvt_pk_bf16_f32 v171, v110, v111
	v_cvt_pk_bf16_f32 v164, v80, v81
	v_cvt_pk_bf16_f32 v165, v82, v83
	v_cvt_pk_bf16_f32 v166, v84, v85
	v_cvt_pk_bf16_f32 v167, v86, v87
	v_cvt_pk_bf16_f32 v160, v88, v89
	v_cvt_pk_bf16_f32 v161, v90, v91
	v_cvt_pk_bf16_f32 v162, v92, v93
	v_cvt_pk_bf16_f32 v163, v94, v95
	s_mul_i32 s47, s26, 0x6000
	s_addk_i32 s93, 0xc000
	s_cmp_lg_u32 s26, 0
	s_cselect_b32 s46, s93, 0x8000
	v_add_u32_e32 v227, s46, v202
	v_add_u32_e32 v207, s47, v185
	v_add_u32_e32 v224, s47, v187
	v_add_u32_e32 v225, s47, v205
	v_add_u32_e32 v226, s47, v206
	s_waitcnt lgkmcnt(0)
	ds_read_b64_tr_b16 v[208:209], v227 offset:0
	ds_read_b64_tr_b16 v[210:211], v227 offset:2048
	ds_read_b64_tr_b16 v[212:213], v227 offset:512
	ds_read_b64_tr_b16 v[214:215], v227 offset:2560
	ds_read_b64_tr_b16 v[216:217], v227 offset:1024
	ds_read_b64_tr_b16 v[218:219], v227 offset:3072
	ds_read_b64_tr_b16 v[220:221], v227 offset:1536
	ds_read_b64_tr_b16 v[222:223], v227 offset:3584
	s_barrier
; template <int DQK, bool HASQK, bool HASPV, int J>
; __device__ __forceinline__ void slot_read(bf16x8 (&kf)[DQK / 16][2], s16x4 (&vf)[4][8], const int (&ka_)[4], int vb_) {
;     constexpr int NQS = HASQK ? 2 * (DQK / 16) : 0, NS = NQS + (HASPV ? 16 : 0);
;     if constexpr (J < NQS) { constexpr int d0 = J >> 1, h = J & 1; dsr128<(d0 >> 2) * 128 + h * 32 * DQK * 2>(kf[d0][h], ka_[d0 & 3]); }
;     else if constexpr (J < NS) { constexpr int q = J - NQS, g = q >> 2, d = q & 3; dstr64<v_rd_off(d, g, 0)>(vf[g][2 * d], vb_); dstr64<v_rd_off(d, g, 1)>(vf[g][2 * d + 1], vb_); }
; }
; template <int DQK, bool HASQK, bool HASPV, int J> ...
;     constexpr int NQS = HASQK ? 2 * (DQK / 16) : 0, NS = NQS + (HASPV ? 16 : 0);
;     if constexpr (J < NS) {
;         constexpr int rd1 = (J + 1 < NS) ? ((J + 1 < NQS) ? 1 : 2) : 0, rd2 = (J + 2 < NS) ? ((J + 2 < NQS) ? 1 : 2) : 0, rd3 = (J + 3 < NS) ? ((J + 3 < NQS) ? 1 : 2) : 0, NW = rd1 + rd2 + rd3;
;     ...
;         if constexpr (J < NQS) { constexpr int d0 = J >> 1, h = J & 1;
;             LWN1(kf[d0][h]); SBAR();
;             if constexpr (h == 0) p0 = __builtin_amdgcn_mfma_f32_32x32x16_bf16(kf[d0][0], qr[d0], (d0 == 0) ? negm : p0, 0, 0, 0);
;             else p1 = __builtin_amdgcn_mfma_f32_32x32x16_bf16(kf[d0][1], qr[d0], (d0 == 0) ? negm : p1, 0, 0, 0);
;         } else { constexpr int q = J - NQS, g = q >> 2, d = q & 3;
;             LWN2(vf[g][2 * d], vf[g][2 * d + 1]); SBAR();
;             o[d] = __builtin_amdgcn_mfma_f32_32x32x16_bf16(pa[g], (bf16x8){vf[g][2 * d][0], vf[g][2 * d][1], vf[g][2 * d][2], vf[g][2 * d][3], vf[g][2 * d + 1][0], vf[g][2 * d + 1][1], vf[g][2 * d + 1][2], vf[g][2 * d + 1][3]}, o[d], 0, 0, 0);
;         }
;     ...
;         SBAR();
;         slot_read<DQK, HASQK, HASPV, J + 4>(kf, vf, ka_, vb_);
;         SBAR();
;         slot_run<DQK, HASQK, HASPV, J + 1>(kf, vf, ka_, vb_, qr, p0, p1, negm, o, pa);
;     }
; }
;     ...
;     for (int i = 0; i < NT - 1; ++i) {
;         SEG_S(i);
;         { const int cp = (ci == 0) ? 2 : ci - 1, cn = (ci == 2) ? 0 : ci + 1;
;           if (DMA_M) { if (i + 3 < NT) DMA_K(i + 3, cp); if (i + 2 < NT) DMA_V(i + 2, cn); }
;           SEG_M(true, true, ci, cp);
;           if (DMA_M && i + 3 < NT) asm volatile("s_waitcnt vmcnt(%0)" :: "n"(NKW + 2) : "memory");
;           else asm volatile("s_waitcnt vmcnt(0)" ::: "memory");
;           BAR_ALL(); }
	s_waitcnt lgkmcnt(6)
	v_mfma_f32_32x32x16_bf16 v[64:79], v[172:175], v[208:211], v[64:79]
	ds_read_b64_tr_b16 v[208:209], v227 offset:4096
	ds_read_b64_tr_b16 v[210:211], v227 offset:6144
	s_waitcnt lgkmcnt(6)
	v_mfma_f32_32x32x16_bf16 v[48:63], v[172:175], v[212:215], v[48:63]
	ds_read_b64_tr_b16 v[212:213], v227 offset:4608
	ds_read_b64_tr_b16 v[214:215], v227 offset:6656
	s_waitcnt lgkmcnt(6)
	v_mfma_f32_32x32x16_bf16 v[32:47], v[172:175], v[216:219], v[32:47]
	ds_read_b64_tr_b16 v[216:217], v227 offset:5120
	ds_read_b64_tr_b16 v[218:219], v227 offset:7168
	s_waitcnt lgkmcnt(6)
	v_mfma_f32_32x32x16_bf16 v[16:31], v[172:175], v[220:223], v[16:31]
	ds_read_b64_tr_b16 v[220:221], v227 offset:5632
	ds_read_b64_tr_b16 v[222:223], v227 offset:7680
	s_waitcnt lgkmcnt(6)
	v_mfma_f32_32x32x16_bf16 v[64:79], v[168:171], v[208:211], v[64:79]
	ds_read_b64_tr_b16 v[208:209], v227 offset:8192
	ds_read_b64_tr_b16 v[210:211], v227 offset:10240
	s_waitcnt lgkmcnt(6)
	v_mfma_f32_32x32x16_bf16 v[48:63], v[168:171], v[212:215], v[48:63]
	ds_read_b64_tr_b16 v[212:213], v227 offset:8704
	ds_read_b64_tr_b16 v[214:215], v227 offset:10752
	s_waitcnt lgkmcnt(6)
	v_mfma_f32_32x32x16_bf16 v[32:47], v[168:171], v[216:219], v[32:47]
	ds_read_b64_tr_b16 v[216:217], v227 offset:9216
	ds_read_b64_tr_b16 v[218:219], v227 offset:11264
	s_waitcnt lgkmcnt(6)
	v_mfma_f32_32x32x16_bf16 v[16:31], v[168:171], v[220:223], v[16:31]
	ds_read_b64_tr_b16 v[220:221], v227 offset:9728
	ds_read_b64_tr_b16 v[222:223], v227 offset:11776
	s_waitcnt lgkmcnt(6)
	v_mfma_f32_32x32x16_bf16 v[64:79], v[164:167], v[208:211], v[64:79]
	ds_read_b64_tr_b16 v[208:209], v227 offset:12288
	ds_read_b64_tr_b16 v[210:211], v227 offset:14336
	s_waitcnt lgkmcnt(6)
	v_mfma_f32_32x32x16_bf16 v[48:63], v[164:167], v[212:215], v[48:63]
	ds_read_b64_tr_b16 v[212:213], v227 offset:12800
	ds_read_b64_tr_b16 v[214:215], v227 offset:14848
	s_waitcnt lgkmcnt(6)
	v_mfma_f32_32x32x16_bf16 v[32:47], v[164:167], v[216:219], v[32:47]
	ds_read_b64_tr_b16 v[216:217], v227 offset:13312
	ds_read_b64_tr_b16 v[218:219], v227 offset:15360
	s_waitcnt lgkmcnt(6)
	v_mfma_f32_32x32x16_bf16 v[16:31], v[164:167], v[220:223], v[16:31]
	ds_read_b64_tr_b16 v[220:221], v227 offset:13824
	ds_read_b64_tr_b16 v[222:223], v227 offset:15872
	v_xor_b32_e32 v80, 0x80000000, v203
	v_mov_b32_e32 v81, v80
	v_mov_b32_e32 v82, v80
	v_mov_b32_e32 v83, v80
	v_mov_b32_e32 v84, v80
	v_mov_b32_e32 v85, v80
	v_mov_b32_e32 v86, v80
	v_mov_b32_e32 v87, v80
	v_mov_b32_e32 v88, v80
	v_mov_b32_e32 v89, v80
	v_mov_b32_e32 v90, v80
	v_mov_b32_e32 v91, v80
	v_mov_b32_e32 v92, v80
	v_mov_b32_e32 v93, v80
	v_mov_b32_e32 v94, v80
	v_mov_b32_e32 v95, v80
	s_waitcnt lgkmcnt(6)
	v_mfma_f32_32x32x16_bf16 v[64:79], v[160:163], v[208:211], v[64:79]
	ds_read_b128 v[208:211], v207 offset:0
	s_waitcnt lgkmcnt(5)
	v_mfma_f32_32x32x16_bf16 v[48:63], v[160:163], v[212:215], v[48:63]
	ds_read_b128 v[212:215], v207 offset:12288
	s_waitcnt lgkmcnt(4)
	v_mfma_f32_32x32x16_bf16 v[32:47], v[160:163], v[216:219], v[32:47]
	ds_read_b128 v[216:219], v224 offset:0
	s_waitcnt lgkmcnt(3)
	v_mfma_f32_32x32x16_bf16 v[16:31], v[160:163], v[220:223], v[16:31]
	ds_read_b128 v[220:223], v224 offset:12288
	s_waitcnt lgkmcnt(3)
	v_mfma_f32_32x32x16_bf16 v[96:111], v[208:211], v[112:115], v[80:95]
	ds_read_b128 v[208:211], v225 offset:0
	s_waitcnt lgkmcnt(3)
	v_mfma_f32_32x32x16_bf16 v[80:95], v[212:215], v[112:115], v[80:95]
	ds_read_b128 v[212:215], v225 offset:12288
	s_waitcnt lgkmcnt(3)
	v_mfma_f32_32x32x16_bf16 v[96:111], v[216:219], v[116:119], v[96:111]
	ds_read_b128 v[216:219], v226 offset:0
	s_waitcnt lgkmcnt(3)
	v_mfma_f32_32x32x16_bf16 v[80:95], v[220:223], v[116:119], v[80:95]
	ds_read_b128 v[220:223], v226 offset:12288
	s_waitcnt lgkmcnt(3)
	v_mfma_f32_32x32x16_bf16 v[96:111], v[208:211], v[120:123], v[96:111]
	ds_read_b128 v[208:211], v207 offset:128
	s_waitcnt lgkmcnt(3)
	v_mfma_f32_32x32x16_bf16 v[80:95], v[212:215], v[120:123], v[80:95]
	ds_read_b128 v[212:215], v207 offset:12416
	s_waitcnt lgkmcnt(3)
	v_mfma_f32_32x32x16_bf16 v[96:111], v[216:219], v[124:127], v[96:111]
	ds_read_b128 v[216:219], v224 offset:128
	s_waitcnt lgkmcnt(3)
	v_mfma_f32_32x32x16_bf16 v[80:95], v[220:223], v[124:127], v[80:95]
	ds_read_b128 v[220:223], v224 offset:12416
	s_waitcnt lgkmcnt(3)
	v_mfma_f32_32x32x16_bf16 v[96:111], v[208:211], v[128:131], v[96:111]
	ds_read_b128 v[208:211], v225 offset:128
	s_waitcnt lgkmcnt(3)
	v_mfma_f32_32x32x16_bf16 v[80:95], v[212:215], v[128:131], v[80:95]
	ds_read_b128 v[212:215], v225 offset:12416
	s_waitcnt lgkmcnt(3)
	v_mfma_f32_32x32x16_bf16 v[96:111], v[216:219], v[132:135], v[96:111]
	ds_read_b128 v[216:219], v226 offset:128
	s_waitcnt lgkmcnt(3)
	v_mfma_f32_32x32x16_bf16 v[80:95], v[220:223], v[132:135], v[80:95]
	ds_read_b128 v[220:223], v226 offset:12416
	s_waitcnt lgkmcnt(3)
	v_mfma_f32_32x32x16_bf16 v[96:111], v[208:211], v[136:139], v[96:111]
	ds_read_b128 v[208:211], v207 offset:256
	s_waitcnt lgkmcnt(3)
	v_mfma_f32_32x32x16_bf16 v[80:95], v[212:215], v[136:139], v[80:95]
	ds_read_b128 v[212:215], v207 offset:12544
	s_waitcnt lgkmcnt(3)
	v_mfma_f32_32x32x16_bf16 v[96:111], v[216:219], v[140:143], v[96:111]
	ds_read_b128 v[216:219], v224 offset:256
	s_waitcnt lgkmcnt(3)
	v_mfma_f32_32x32x16_bf16 v[80:95], v[220:223], v[140:143], v[80:95]
	ds_read_b128 v[220:223], v224 offset:12544
	s_waitcnt lgkmcnt(3)
	v_mfma_f32_32x32x16_bf16 v[96:111], v[208:211], v[144:147], v[96:111]
	ds_read_b128 v[208:211], v225 offset:256
	s_waitcnt lgkmcnt(3)
	v_mfma_f32_32x32x16_bf16 v[80:95], v[212:215], v[144:147], v[80:95]
	ds_read_b128 v[212:215], v225 offset:12544
	s_waitcnt lgkmcnt(3)
	v_mfma_f32_32x32x16_bf16 v[96:111], v[216:219], v[148:151], v[96:111]
	ds_read_b128 v[216:219], v226 offset:256
	s_waitcnt lgkmcnt(3)
	v_mfma_f32_32x32x16_bf16 v[80:95], v[220:223], v[148:151], v[80:95]
	ds_read_b128 v[220:223], v226 offset:12544
	s_waitcnt lgkmcnt(3)
	v_mfma_f32_32x32x16_bf16 v[96:111], v[208:211], v[152:155], v[96:111]
	s_waitcnt lgkmcnt(2)
	v_mfma_f32_32x32x16_bf16 v[80:95], v[212:215], v[152:155], v[80:95]
	s_waitcnt lgkmcnt(1)
	v_mfma_f32_32x32x16_bf16 v[96:111], v[216:219], v[156:159], v[96:111]
	s_waitcnt lgkmcnt(0)
	v_mfma_f32_32x32x16_bf16 v[80:95], v[220:223], v[156:159], v[80:95]
	s_waitcnt vmcnt(0)
	s_waitcnt lgkmcnt(0)
	s_barrier
	s_add_u32 s44, s44, 0x18000
	s_addc_u32 s45, s45, 0
	s_add_u32 s100, s100, 0x10000
	s_addc_u32 s101, s101, 0
	s_cmp_eq_u32 s44, 0xbe8000
	s_cbranch_scc1 .LBB0_616

; __device__ __forceinline__ float vmax3(float x, float y, float z) { float r; asm("v_max3_f32 %0, %1, %2, %3" : "=v"(r) : "v"(x), "v"(y), "v"(z)); return r; }
; __device__ __forceinline__ float vmax2(float x, float y) { float r; asm("v_max_f32 %0, %1, %2" : "=v"(r) : "v"(x), "v"(y)); return r; }
; __device__ __forceinline__ void smax_tile(f32x16& p0, f32x16& p1, float& mhat, float& l_reg, f32x16 (&o)[4], float* al_l, const bool first, int r32, int hi,
;                                           bf16x8& pa0, bf16x8& pa1, bf16x8& pa2, bf16x8& pa3) {
;     float a = vmax3(p0[0], p0[1], p1[0]), b = vmax3(p0[2], p0[3], p1[1]); a = vmax3(a, p1[2], p1[3]);
; #pragma unroll
;     for (int r = 4; r < 16; r += 4) { a = vmax3(a, p0[r], p0[r + 1]); b = vmax3(b, p0[r + 2], p0[r + 3]); a = vmax3(a, p1[r], p1[r + 1]); b = vmax3(b, p1[r + 2], p1[r + 3]); }
;     float rm = vmax2(a, b);
;     { auto rr = __builtin_amdgcn_permlane32_swap(__float_as_uint(rm), __float_as_uint(rm), false, false); rm = vmax2(__uint_as_float(rr[0]), __uint_as_float(rr[1])); }
;     if (__builtin_expect(first || __any(rm > THRL), 0)) {
.LBB0_608:
	s_mov_b32 m0, s47
	v_max3_f32 v160, v96, v97, v80
	global_load_lds_dwordx4 v228, s[100:101]
	s_add_i32 m0, s47, 0x400
	v_max3_f32 v161, v98, v99, v81
	global_load_lds_dwordx4 v229, s[100:101]
	v_max3_f32 v160, v160, v82, v83
	v_max3_f32 v161, v161, v102, v103
	v_max3_f32 v160, v160, v100, v101
	v_max3_f32 v161, v161, v86, v87
	v_max3_f32 v160, v160, v84, v85
	v_max3_f32 v161, v161, v106, v107
	v_max3_f32 v160, v160, v104, v105
	v_max3_f32 v161, v161, v90, v91
	v_max3_f32 v160, v160, v88, v89
	v_max3_f32 v161, v161, v110, v111
	v_max3_f32 v160, v160, v108, v109
	v_max3_f32 v161, v161, v94, v95
	v_max3_f32 v160, v160, v92, v93
	v_max_f32 v160, v160, v161
	v_mov_b32_e32 v161, v160
	s_nop 0
	s_cmp_eq_u32 s44, 0
	v_permlane32_swap_b32_e32 v160, v161
	v_max_f32 v160, v160, v161
	s_cbranch_scc1 .LBB0_615
	v_cmp_lt_f32_e32 vcc, s87, v160
	s_cbranch_vccz .LBB0_605
	s_branch .LBB0_614

; __global__ void __launch_bounds__(512, 2) hymba_fwd(Args args) {
	.amdhsa_kernel _Z9hymba_fwd4Args
		.amdhsa_group_segment_fixed_size 0
		.amdhsa_private_segment_fixed_size 0
		.amdhsa_kernarg_size 472
		.amdhsa_user_sgpr_count 2
		.amdhsa_user_sgpr_dispatch_ptr 0
		.amdhsa_user_sgpr_queue_ptr 0
		.amdhsa_user_sgpr_kernarg_segment_ptr 1
		.amdhsa_user_sgpr_dispatch_id 0
		.amdhsa_user_sgpr_kernarg_preload_length 0
		.amdhsa_user_sgpr_kernarg_preload_offset 0
		.amdhsa_user_sgpr_private_segment_size 0
		.amdhsa_uses_dynamic_stack 0
		.amdhsa_enable_private_segment 0
		.amdhsa_system_sgpr_workgroup_id_x 1
		.amdhsa_system_sgpr_workgroup_id_y 0
		.amdhsa_system_sgpr_workgroup_id_z 0
		.amdhsa_system_sgpr_workgroup_info 0
		.amdhsa_system_vgpr_workitem_id 0
		.amdhsa_next_free_vgpr 249
		.amdhsa_next_free_sgpr 102
		.amdhsa_accum_offset 252
		.amdhsa_reserve_vcc 1
		.amdhsa_float_round_mode_32 0
		.amdhsa_float_round_mode_16_64 0
		.amdhsa_float_denorm_mode_32 3
		.amdhsa_float_denorm_mode_16_64 3
		.amdhsa_dx10_clamp 1
		.amdhsa_ieee_mode 1
		.amdhsa_fp16_overflow 0
		.amdhsa_tg_split 0
		.amdhsa_exception_fp_ieee_invalid_op 0
		.amdhsa_exception_fp_denorm_src 0
		.amdhsa_exception_fp_ieee_div_zero 0
		.amdhsa_exception_fp_ieee_overflow 0
		.amdhsa_exception_fp_ieee_underflow 0
		.amdhsa_exception_fp_ieee_inexact 0
		.amdhsa_exception_int_div_zero 0
	.end_amdhsa_kernel
